# baseline (speedup 1.0000x reference)
.Lrk_top:
	v_sub_f32_e32 v238, 1.0, v221
	v_min_f32_e32 v178, v1, v238
	v_cmp_eq_f32_e32 vcc, 0, v178
	v_mul_f32_e32 v178, 0x3b000000, v178
	s_cmp_eq_u64 vcc, exec
	s_cbranch_scc1 .Lrk_exit
	s_cmp_gt_i32 s30, 63
	s_cbranch_scc1 .Lrk_exit
	v_mul_f32_e32 v134, 0x3e4ccccd, v173
	v_mul_f32_e32 v142, 0x3e4ccccd, v172
	v_mul_f32_e32 v150, 0x3e4ccccd, v175
	v_mul_f32_e32 v158, 0x3e4ccccd, v174
	v_fma_mixlo_f16 v131, v178, v134, v171
	v_fma_mixlo_f16 v139, v178, v142, v170
	v_fma_mixlo_f16 v147, v178, v150, v169
	v_fma_mixlo_f16 v155, v178, v158, v168
	v_fma_f32 v130, v178, v134, v171
	v_fma_f32 v138, v178, v142, v170
	v_fma_f32 v146, v178, v150, v169
	v_fma_f32 v154, v178, v158, v168
	v_fma_mix_f32 v130, v130, 1.0, -v131 op_sel_hi:[0,0,1]
	v_fma_mix_f32 v138, v138, 1.0, -v139 op_sel_hi:[0,0,1]
	v_fma_mix_f32 v146, v146, 1.0, -v147 op_sel_hi:[0,0,1]
	v_fma_mix_f32 v154, v154, 1.0, -v155 op_sel_hi:[0,0,1]
	v_fma_mixlo_f16 v133, v130, s42, 0
	v_fma_mixlo_f16 v141, v138, s42, 0
	v_fma_mixlo_f16 v149, v146, s42, 0
	v_fma_mixlo_f16 v157, v154, s42, 0
	v_fma_mix_f32 v130, v130, s42, -v133 op_sel_hi:[0,0,1]
	v_fma_mix_f32 v138, v138, s42, -v141 op_sel_hi:[0,0,1]
	v_fma_mix_f32 v146, v146, s42, -v149 op_sel_hi:[0,0,1]
	v_fma_mix_f32 v154, v154, s42, -v157 op_sel_hi:[0,0,1]
	v_fma_mixlo_f16 v132, v130, s42, 0
	v_fma_mixlo_f16 v140, v138, s42, 0
	v_fma_mixlo_f16 v148, v146, s42, 0
	v_fma_mixlo_f16 v156, v154, s42, 0
	ds_write_b16 v204, v131
	ds_write_b16 v205, v139
	ds_write_b16 v206, v147
	ds_write_b16 v207, v155
	ds_write_b16 v204, v133 offset:544
	ds_write_b16 v205, v141 offset:544
	ds_write_b16 v206, v149 offset:544
	ds_write_b16 v207, v157 offset:544
	ds_write_b16 v204, v132 offset:1088
	ds_write_b16 v205, v140 offset:1088
	ds_write_b16 v206, v148 offset:1088
	ds_write_b16 v207, v156 offset:1088
	s_waitcnt lgkmcnt(0)
	s_barrier
	ds_read_b128 v[130:133], v208
	ds_read_b128 v[134:137], v209 offset:64
	ds_read_b128 v[138:141], v211
	ds_read_b128 v[142:145], v212
	ds_read_b128 v[146:149], v213
	ds_read_b128 v[150:153], v214
	ds_read_b128 v[154:157], v215
	ds_read_b128 v[158:161], v216
	ds_read_b128 v[180:183], v199 offset:0
	ds_read_b128 v[184:187], v199 offset:1024
	ds_read_b128 v[188:191], v199 offset:4096
	ds_read_b128 v[192:195], v199 offset:5120
	ds_read_b128 v[222:225], v199 offset:8192
	s_waitcnt lgkmcnt(6)
	ds_read_b128 v[226:229], v199 offset:9216
	v_smfmac_f32_16x16x64_f16 v[230:233], v[130:133], a[0:7], v210
	ds_read_b128 v[238:241], v217
	v_smfmac_f32_16x16x64_f16 v[234:237], v[130:133], v[18:25], v210
	ds_read_b128 v[242:245], v217
	v_smfmac_f32_16x16x64_f16 v[230:233], v[134:137], a[40:47], v210
	v_mul_f32_e32 v166, 0x3d99999a, v173
	v_smfmac_f32_16x16x64_f16 v[234:237], v[134:137], v[34:41], v210
	v_mul_f32_e32 v167, 0x3d99999a, v172
	v_smfmac_f32_16x16x64_f16 v[230:233], v[138:141], a[64:71], v210
	v_mul_f32_e32 v176, 0x3d99999a, v175
	v_smfmac_f32_16x16x64_f16 v[234:237], v[138:141], v[42:49], v210
	v_mul_f32_e32 v177, 0x3d99999a, v174
	v_smfmac_f32_16x16x64_f16 v[230:233], v[142:145], a[96:103], v210
	v_smfmac_f32_16x16x64_f16 v[234:237], v[142:145], v[58:65], v210
	v_smfmac_f32_16x16x64_f16 v[230:233], v[146:149], a[128:135], v210
	v_smfmac_f32_16x16x64_f16 v[234:237], v[146:149], v[74:81], v210
	v_smfmac_f32_16x16x64_f16 v[230:233], v[150:153], a[160:167], v210
	v_smfmac_f32_16x16x64_f16 v[234:237], v[150:153], v[98:105], v210
	v_smfmac_f32_16x16x64_f16 v[230:233], v[154:157], a[192:199], v210
	v_smfmac_f32_16x16x64_f16 v[234:237], v[154:157], v[106:113], v210
	s_waitcnt lgkmcnt(8)
	v_smfmac_f32_16x16x64_f16 v[230:233], v[158:161], a[224:231], v210
	v_smfmac_f32_16x16x64_f16 v[234:237], v[158:161], v[122:129], v210
	s_waitcnt lgkmcnt(1)
	v_smfmac_f32_16x16x64_f16 v[238:241], v[130:133], a[16:23], v210
	s_waitcnt lgkmcnt(0)
	v_smfmac_f32_16x16x64_f16 v[242:245], v[130:133], v[180:187], v210
	ds_read_b128 v[180:183], v199 offset:12288
	ds_read_b128 v[184:187], v199 offset:13312
	v_smfmac_f32_16x16x64_f16 v[238:241], v[134:137], a[48:55], v210
	v_fmac_f32_e32 v230, s40, v231
	v_fmac_f32_e32 v234, s40, v235
	v_smfmac_f32_16x16x64_f16 v[242:245], v[134:137], v[188:195], v210
	ds_read_b128 v[188:191], v199 offset:16384
	ds_read_b128 v[192:195], v199 offset:17408
	v_fmac_f32_e32 v230, s41, v232
	v_fmac_f32_e32 v234, s41, v236
	v_smfmac_f32_16x16x64_f16 v[238:241], v[138:141], a[80:87], v210
	s_nop 0
	v_permlane32_swap_b32_e32 v230, v234
	v_add_f32_e32 v162, v230, v234
	v_smfmac_f32_16x16x64_f16 v[242:245], v[138:141], v[222:229], v210
	ds_read_b128 v[222:225], v199 offset:20480
	ds_read_b128 v[226:229], v199 offset:21504
	v_fmac_f32_e32 v166, 0x3e666666, v162
	v_fma_mixlo_f16 v232, v178, v166, v171
	v_smfmac_f32_16x16x64_f16 v[238:241], v[142:145], a[112:119], v210
	v_fma_f32 v231, v178, v166, v171
	v_fma_mix_f32 v231, v231, 1.0, -v232 op_sel_hi:[0,0,1]
	s_waitcnt lgkmcnt(4)
	v_smfmac_f32_16x16x64_f16 v[242:245], v[142:145], v[180:187], v210
	ds_read_b128 v[180:183], v199 offset:24576
	ds_read_b128 v[184:187], v199 offset:25600
	v_fma_mixlo_f16 v235, v231, s42, 0
	v_smfmac_f32_16x16x64_f16 v[238:241], v[146:149], a[144:151], v210
	v_fma_mix_f32 v231, v231, s42, -v235 op_sel_hi:[0,0,1]
	s_waitcnt lgkmcnt(4)
	v_smfmac_f32_16x16x64_f16 v[242:245], v[146:149], v[188:195], v210
	ds_read_b128 v[188:191], v199 offset:28672
	ds_read_b128 v[192:195], v199 offset:29696
	v_fma_mixlo_f16 v233, v231, s42, 0
	v_smfmac_f32_16x16x64_f16 v[238:241], v[150:153], a[176:183], v210
	ds_write_b16 v204, v232 offset:8704
	s_waitcnt lgkmcnt(5)
	v_smfmac_f32_16x16x64_f16 v[242:245], v[150:153], v[222:229], v210
	ds_read_b128 v[222:225], v199 offset:2048
	ds_read_b128 v[226:229], v199 offset:3072
	ds_write_b16 v204, v235 offset:9248
	v_smfmac_f32_16x16x64_f16 v[238:241], v[154:157], a[208:215], v210
	ds_write_b16 v204, v233 offset:9792
	s_waitcnt lgkmcnt(7)
	v_smfmac_f32_16x16x64_f16 v[242:245], v[154:157], v[180:187], v210
	ds_read_b128 v[180:183], v199 offset:6144
	ds_read_b128 v[184:187], v199 offset:7168
	ds_read_b128 v[230:233], v217
	v_smfmac_f32_16x16x64_f16 v[238:241], v[158:161], a[240:247], v210
	ds_read_b128 v[234:237], v217
	s_waitcnt lgkmcnt(9)
	v_smfmac_f32_16x16x64_f16 v[242:245], v[158:161], v[188:195], v210
	ds_read_b128 v[188:191], v199 offset:10240
	ds_read_b128 v[192:195], v199 offset:11264
	s_waitcnt lgkmcnt(3)
	v_smfmac_f32_16x16x64_f16 v[230:233], v[130:133], a[8:15], v210
	s_waitcnt lgkmcnt(2)
	v_smfmac_f32_16x16x64_f16 v[234:237], v[130:133], v[2:9], v210
	v_smfmac_f32_16x16x64_f16 v[230:233], v[134:137], a[32:39], v210
	v_fmac_f32_e32 v238, s40, v239
	v_fmac_f32_e32 v242, s40, v243
	v_smfmac_f32_16x16x64_f16 v[234:237], v[134:137], v[10:17], v210
	v_fmac_f32_e32 v238, s41, v240
	v_fmac_f32_e32 v242, s41, v244
	v_smfmac_f32_16x16x64_f16 v[230:233], v[138:141], a[72:79], v210
	s_nop 0
	v_permlane32_swap_b32_e32 v238, v242
	v_add_f32_e32 v164, v238, v242
	v_smfmac_f32_16x16x64_f16 v[234:237], v[138:141], v[50:57], v210
	v_fmac_f32_e32 v176, 0x3e666666, v164
	v_fma_mixlo_f16 v240, v178, v176, v169
	v_smfmac_f32_16x16x64_f16 v[230:233], v[142:145], a[104:111], v210
	v_fma_f32 v239, v178, v176, v169
	v_fma_mix_f32 v239, v239, 1.0, -v240 op_sel_hi:[0,0,1]
	v_smfmac_f32_16x16x64_f16 v[234:237], v[142:145], v[26:33], v210
	v_fma_mixlo_f16 v243, v239, s42, 0
	v_smfmac_f32_16x16x64_f16 v[230:233], v[146:149], a[136:143], v210
	v_fma_mix_f32 v239, v239, s42, -v243 op_sel_hi:[0,0,1]
	v_smfmac_f32_16x16x64_f16 v[234:237], v[146:149], v[82:89], v210
	v_fma_mixlo_f16 v241, v239, s42, 0
	v_smfmac_f32_16x16x64_f16 v[230:233], v[150:153], a[168:175], v210
	ds_write_b16 v206, v240 offset:8704
	v_smfmac_f32_16x16x64_f16 v[234:237], v[150:153], v[66:73], v210
	ds_write_b16 v206, v243 offset:9248
	v_smfmac_f32_16x16x64_f16 v[230:233], v[154:157], a[200:207], v210
	ds_write_b16 v206, v241 offset:9792
	v_smfmac_f32_16x16x64_f16 v[234:237], v[154:157], v[114:121], v210
	ds_read_b128 v[238:241], v217
	v_smfmac_f32_16x16x64_f16 v[230:233], v[158:161], a[232:239], v210
	ds_read_b128 v[242:245], v217
	v_smfmac_f32_16x16x64_f16 v[234:237], v[158:161], v[90:97], v210
	s_waitcnt lgkmcnt(1)
	v_smfmac_f32_16x16x64_f16 v[238:241], v[130:133], a[24:31], v210
	s_waitcnt lgkmcnt(0)
	v_smfmac_f32_16x16x64_f16 v[242:245], v[130:133], v[222:229], v210
	ds_read_b128 v[222:225], v199 offset:14336
	ds_read_b128 v[226:229], v199 offset:15360
	v_smfmac_f32_16x16x64_f16 v[238:241], v[134:137], a[56:63], v210
	v_fmac_f32_e32 v230, s40, v231
	v_fmac_f32_e32 v234, s40, v235
	v_smfmac_f32_16x16x64_f16 v[242:245], v[134:137], v[180:187], v210
	ds_read_b128 v[180:183], v199 offset:18432
	ds_read_b128 v[184:187], v199 offset:19456
	v_fmac_f32_e32 v230, s41, v232
	v_fmac_f32_e32 v234, s41, v236
	v_smfmac_f32_16x16x64_f16 v[238:241], v[138:141], a[88:95], v210
	s_nop 0
	v_permlane32_swap_b32_e32 v230, v234
	v_add_f32_e32 v163, v230, v234
	v_smfmac_f32_16x16x64_f16 v[242:245], v[138:141], v[188:195], v210
	ds_read_b128 v[188:191], v199 offset:22528
	ds_read_b128 v[192:195], v199 offset:23552
	v_fmac_f32_e32 v167, 0x3e666666, v163
	v_fma_mixlo_f16 v232, v178, v167, v170
	v_smfmac_f32_16x16x64_f16 v[238:241], v[142:145], a[120:127], v210
	v_fma_f32 v231, v178, v167, v170
	v_fma_mix_f32 v231, v231, 1.0, -v232 op_sel_hi:[0,0,1]
	s_waitcnt lgkmcnt(4)
	v_smfmac_f32_16x16x64_f16 v[242:245], v[142:145], v[222:229], v210
	ds_read_b128 v[222:225], v199 offset:26624
	ds_read_b128 v[226:229], v199 offset:27648
	v_fma_mixlo_f16 v235, v231, s42, 0
	v_smfmac_f32_16x16x64_f16 v[238:241], v[146:149], a[152:159], v210
	v_fma_mix_f32 v231, v231, s42, -v235 op_sel_hi:[0,0,1]
	s_waitcnt lgkmcnt(4)
	v_smfmac_f32_16x16x64_f16 v[242:245], v[146:149], v[180:187], v210
	ds_read_b128 v[180:183], v199 offset:30720
	ds_read_b128 v[184:187], v199 offset:31744
	v_fma_mixlo_f16 v233, v231, s42, 0
	v_smfmac_f32_16x16x64_f16 v[238:241], v[150:153], a[184:191], v210
	ds_write_b16 v205, v232 offset:8704
	s_waitcnt lgkmcnt(5)
	v_smfmac_f32_16x16x64_f16 v[242:245], v[150:153], v[188:195], v210
	ds_write_b16 v205, v235 offset:9248
	v_smfmac_f32_16x16x64_f16 v[238:241], v[154:157], a[216:223], v210
	ds_write_b16 v205, v233 offset:9792
	s_waitcnt lgkmcnt(5)
	v_smfmac_f32_16x16x64_f16 v[242:245], v[154:157], v[222:229], v210
	ds_read_b128 v[230:233], v217
	v_smfmac_f32_16x16x64_f16 v[238:241], v[158:161], a[248:255], v210
	ds_read_b128 v[234:237], v217
	s_waitcnt lgkmcnt(5)
	v_smfmac_f32_16x16x64_f16 v[242:245], v[158:161], v[180:187], v210
	s_nop 4
	v_fmac_f32_e32 v238, s40, v239
	s_nop 1
	v_fmac_f32_e32 v242, s40, v243
	v_fmac_f32_e32 v238, s41, v240
	v_fmac_f32_e32 v242, s41, v244
	s_nop 1
	v_permlane32_swap_b32_e32 v238, v242
	v_add_f32_e32 v165, v238, v242
	v_fmac_f32_e32 v177, 0x3e666666, v165
	v_fma_mixlo_f16 v240, v178, v177, v168
	v_fma_f32 v239, v178, v177, v168
	v_fma_mix_f32 v239, v239, 1.0, -v240 op_sel_hi:[0,0,1]
	v_fma_mixlo_f16 v243, v239, s42, 0
	v_fma_mix_f32 v239, v239, s42, -v243 op_sel_hi:[0,0,1]
	v_fma_mixlo_f16 v241, v239, s42, 0
	ds_write_b16 v207, v240 offset:8704
	ds_write_b16 v207, v243 offset:9248
	ds_write_b16 v207, v241 offset:9792
	s_waitcnt lgkmcnt(0)
	s_barrier
	ds_read_b128 v[130:133], v208 offset:8704
	ds_read_b128 v[134:137], v209 offset:8768
	ds_read_b128 v[138:141], v211 offset:8704
	ds_read_b128 v[142:145], v212 offset:8704
	ds_read_b128 v[146:149], v213 offset:8704
	ds_read_b128 v[150:153], v214 offset:8704
	ds_read_b128 v[154:157], v215 offset:8704
	ds_read_b128 v[158:161], v216 offset:8704
	ds_read_b128 v[180:183], v199 offset:0
	ds_read_b128 v[184:187], v199 offset:1024
	ds_read_b128 v[188:191], v199 offset:4096
	ds_read_b128 v[192:195], v199 offset:5120
	ds_read_b128 v[222:225], v199 offset:8192
	s_waitcnt lgkmcnt(6)
	ds_read_b128 v[226:229], v199 offset:9216
	v_smfmac_f32_16x16x64_f16 v[230:233], v[130:133], a[0:7], v210
	ds_read_b128 v[238:241], v217
	v_smfmac_f32_16x16x64_f16 v[234:237], v[130:133], v[18:25], v210
	ds_read_b128 v[242:245], v217
	v_smfmac_f32_16x16x64_f16 v[230:233], v[134:137], a[40:47], v210
	v_mul_f32_e32 v179, 0x3f7a4fa5, v173
	v_smfmac_f32_16x16x64_f16 v[234:237], v[134:137], v[34:41], v210
	v_fmac_f32_e32 v179, 0xc06eeeef, v162
	v_smfmac_f32_16x16x64_f16 v[230:233], v[138:141], a[64:71], v210
	v_mul_f32_e32 v196, 0x3f7a4fa5, v172
	v_smfmac_f32_16x16x64_f16 v[234:237], v[138:141], v[42:49], v210
	v_fmac_f32_e32 v196, 0xc06eeeef, v163
	v_smfmac_f32_16x16x64_f16 v[230:233], v[142:145], a[96:103], v210
	v_mul_f32_e32 v197, 0x3f7a4fa5, v175
	v_smfmac_f32_16x16x64_f16 v[234:237], v[142:145], v[58:65], v210
	v_fmac_f32_e32 v197, 0xc06eeeef, v164
	v_smfmac_f32_16x16x64_f16 v[230:233], v[146:149], a[128:135], v210
	v_mul_f32_e32 v198, 0x3f7a4fa5, v174
	v_smfmac_f32_16x16x64_f16 v[234:237], v[146:149], v[74:81], v210
	v_fmac_f32_e32 v198, 0xc06eeeef, v165
	v_smfmac_f32_16x16x64_f16 v[230:233], v[150:153], a[160:167], v210
	v_smfmac_f32_16x16x64_f16 v[234:237], v[150:153], v[98:105], v210
	v_smfmac_f32_16x16x64_f16 v[230:233], v[154:157], a[192:199], v210
	v_smfmac_f32_16x16x64_f16 v[234:237], v[154:157], v[106:113], v210
	s_waitcnt lgkmcnt(8)
	v_smfmac_f32_16x16x64_f16 v[230:233], v[158:161], a[224:231], v210
	v_smfmac_f32_16x16x64_f16 v[234:237], v[158:161], v[122:129], v210
	s_waitcnt lgkmcnt(1)
	v_smfmac_f32_16x16x64_f16 v[238:241], v[130:133], a[16:23], v210
	s_waitcnt lgkmcnt(0)
	v_smfmac_f32_16x16x64_f16 v[242:245], v[130:133], v[180:187], v210
	ds_read_b128 v[180:183], v199 offset:12288
	ds_read_b128 v[184:187], v199 offset:13312
	v_smfmac_f32_16x16x64_f16 v[238:241], v[134:137], a[48:55], v210
	v_fmac_f32_e32 v230, s40, v231
	v_fmac_f32_e32 v234, s40, v235
	v_smfmac_f32_16x16x64_f16 v[242:245], v[134:137], v[188:195], v210
	ds_read_b128 v[188:191], v199 offset:16384
	ds_read_b128 v[192:195], v199 offset:17408
	v_fmac_f32_e32 v230, s41, v232
	v_fmac_f32_e32 v234, s41, v236
	v_smfmac_f32_16x16x64_f16 v[238:241], v[138:141], a[80:87], v210
	s_nop 0
	v_permlane32_swap_b32_e32 v230, v234
	v_add_f32_e32 v166, v230, v234
	v_smfmac_f32_16x16x64_f16 v[242:245], v[138:141], v[222:229], v210
	ds_read_b128 v[222:225], v199 offset:20480
	ds_read_b128 v[226:229], v199 offset:21504
	v_fmac_f32_e32 v179, 0x40638e39, v166
	v_fma_mixlo_f16 v232, v178, v179, v171
	v_smfmac_f32_16x16x64_f16 v[238:241], v[142:145], a[112:119], v210
	v_fma_f32 v231, v178, v179, v171
	v_fma_mix_f32 v231, v231, 1.0, -v232 op_sel_hi:[0,0,1]
	s_waitcnt lgkmcnt(4)
	v_smfmac_f32_16x16x64_f16 v[242:245], v[142:145], v[180:187], v210
	ds_read_b128 v[180:183], v199 offset:24576
	ds_read_b128 v[184:187], v199 offset:25600
	v_fma_mixlo_f16 v235, v231, s42, 0
	v_smfmac_f32_16x16x64_f16 v[238:241], v[146:149], a[144:151], v210
	v_fma_mix_f32 v231, v231, s42, -v235 op_sel_hi:[0,0,1]
	s_waitcnt lgkmcnt(4)
	v_smfmac_f32_16x16x64_f16 v[242:245], v[146:149], v[188:195], v210
	ds_read_b128 v[188:191], v199 offset:28672
	ds_read_b128 v[192:195], v199 offset:29696
	v_fma_mixlo_f16 v233, v231, s42, 0
	v_smfmac_f32_16x16x64_f16 v[238:241], v[150:153], a[176:183], v210
	ds_write_b16 v204, v232
	s_waitcnt lgkmcnt(5)
	v_smfmac_f32_16x16x64_f16 v[242:245], v[150:153], v[222:229], v210
	ds_read_b128 v[222:225], v199 offset:2048
	ds_read_b128 v[226:229], v199 offset:3072
	ds_write_b16 v204, v235 offset:544
	v_smfmac_f32_16x16x64_f16 v[238:241], v[154:157], a[208:215], v210
	ds_write_b16 v204, v233 offset:1088
	s_waitcnt lgkmcnt(7)
	v_smfmac_f32_16x16x64_f16 v[242:245], v[154:157], v[180:187], v210
	ds_read_b128 v[180:183], v199 offset:6144
	ds_read_b128 v[184:187], v199 offset:7168
	ds_read_b128 v[230:233], v217
	v_smfmac_f32_16x16x64_f16 v[238:241], v[158:161], a[240:247], v210
	ds_read_b128 v[234:237], v217
	s_waitcnt lgkmcnt(9)
	v_smfmac_f32_16x16x64_f16 v[242:245], v[158:161], v[188:195], v210
	ds_read_b128 v[188:191], v199 offset:10240
	ds_read_b128 v[192:195], v199 offset:11264
	s_waitcnt lgkmcnt(3)
	v_smfmac_f32_16x16x64_f16 v[230:233], v[130:133], a[8:15], v210
	s_waitcnt lgkmcnt(2)
	v_smfmac_f32_16x16x64_f16 v[234:237], v[130:133], v[2:9], v210
	v_smfmac_f32_16x16x64_f16 v[230:233], v[134:137], a[32:39], v210
	v_fmac_f32_e32 v238, s40, v239
	v_fmac_f32_e32 v242, s40, v243
	v_smfmac_f32_16x16x64_f16 v[234:237], v[134:137], v[10:17], v210
	v_fmac_f32_e32 v238, s41, v240
	v_fmac_f32_e32 v242, s41, v244
	v_smfmac_f32_16x16x64_f16 v[230:233], v[138:141], a[72:79], v210
	s_nop 0
	v_permlane32_swap_b32_e32 v238, v242
	v_add_f32_e32 v176, v238, v242
	v_smfmac_f32_16x16x64_f16 v[234:237], v[138:141], v[50:57], v210
	v_fmac_f32_e32 v197, 0x40638e39, v176
	v_fma_mixlo_f16 v240, v178, v197, v169
	v_smfmac_f32_16x16x64_f16 v[230:233], v[142:145], a[104:111], v210
	v_fma_f32 v239, v178, v197, v169
	v_fma_mix_f32 v239, v239, 1.0, -v240 op_sel_hi:[0,0,1]
	v_smfmac_f32_16x16x64_f16 v[234:237], v[142:145], v[26:33], v210
	v_fma_mixlo_f16 v243, v239, s42, 0
	v_smfmac_f32_16x16x64_f16 v[230:233], v[146:149], a[136:143], v210
	v_fma_mix_f32 v239, v239, s42, -v243 op_sel_hi:[0,0,1]
	v_smfmac_f32_16x16x64_f16 v[234:237], v[146:149], v[82:89], v210
	v_fma_mixlo_f16 v241, v239, s42, 0
	v_smfmac_f32_16x16x64_f16 v[230:233], v[150:153], a[168:175], v210
	ds_write_b16 v206, v240
	v_smfmac_f32_16x16x64_f16 v[234:237], v[150:153], v[66:73], v210
	ds_write_b16 v206, v243 offset:544
	v_smfmac_f32_16x16x64_f16 v[230:233], v[154:157], a[200:207], v210
	ds_write_b16 v206, v241 offset:1088
	v_smfmac_f32_16x16x64_f16 v[234:237], v[154:157], v[114:121], v210
	ds_read_b128 v[238:241], v217
	v_smfmac_f32_16x16x64_f16 v[230:233], v[158:161], a[232:239], v210
	ds_read_b128 v[242:245], v217
	v_smfmac_f32_16x16x64_f16 v[234:237], v[158:161], v[90:97], v210
	s_waitcnt lgkmcnt(1)
	v_smfmac_f32_16x16x64_f16 v[238:241], v[130:133], a[24:31], v210
	s_waitcnt lgkmcnt(0)
	v_smfmac_f32_16x16x64_f16 v[242:245], v[130:133], v[222:229], v210
	ds_read_b128 v[222:225], v199 offset:14336
	ds_read_b128 v[226:229], v199 offset:15360
	v_smfmac_f32_16x16x64_f16 v[238:241], v[134:137], a[56:63], v210
	v_fmac_f32_e32 v230, s40, v231
	v_fmac_f32_e32 v234, s40, v235
	v_smfmac_f32_16x16x64_f16 v[242:245], v[134:137], v[180:187], v210
	ds_read_b128 v[180:183], v199 offset:18432
	ds_read_b128 v[184:187], v199 offset:19456
	v_fmac_f32_e32 v230, s41, v232
	v_fmac_f32_e32 v234, s41, v236
	v_smfmac_f32_16x16x64_f16 v[238:241], v[138:141], a[88:95], v210
	s_nop 0
	v_permlane32_swap_b32_e32 v230, v234
	v_add_f32_e32 v167, v230, v234
	v_smfmac_f32_16x16x64_f16 v[242:245], v[138:141], v[188:195], v210
	ds_read_b128 v[188:191], v199 offset:22528
	ds_read_b128 v[192:195], v199 offset:23552
	v_fmac_f32_e32 v196, 0x40638e39, v167
	v_fma_mixlo_f16 v232, v178, v196, v170
	v_smfmac_f32_16x16x64_f16 v[238:241], v[142:145], a[120:127], v210
	v_fma_f32 v231, v178, v196, v170
	v_fma_mix_f32 v231, v231, 1.0, -v232 op_sel_hi:[0,0,1]
	s_waitcnt lgkmcnt(4)
	v_smfmac_f32_16x16x64_f16 v[242:245], v[142:145], v[222:229], v210
	ds_read_b128 v[222:225], v199 offset:26624
	ds_read_b128 v[226:229], v199 offset:27648
	v_fma_mixlo_f16 v235, v231, s42, 0
	v_smfmac_f32_16x16x64_f16 v[238:241], v[146:149], a[152:159], v210
	v_fma_mix_f32 v231, v231, s42, -v235 op_sel_hi:[0,0,1]
	s_waitcnt lgkmcnt(4)
	v_smfmac_f32_16x16x64_f16 v[242:245], v[146:149], v[180:187], v210
	ds_read_b128 v[180:183], v199 offset:30720
	ds_read_b128 v[184:187], v199 offset:31744
	v_fma_mixlo_f16 v233, v231, s42, 0
	v_smfmac_f32_16x16x64_f16 v[238:241], v[150:153], a[184:191], v210
	ds_write_b16 v205, v232
	s_waitcnt lgkmcnt(5)
	v_smfmac_f32_16x16x64_f16 v[242:245], v[150:153], v[188:195], v210
	ds_write_b16 v205, v235 offset:544
	v_smfmac_f32_16x16x64_f16 v[238:241], v[154:157], a[216:223], v210
	ds_write_b16 v205, v233 offset:1088
	s_waitcnt lgkmcnt(5)
	v_smfmac_f32_16x16x64_f16 v[242:245], v[154:157], v[222:229], v210
	ds_read_b128 v[230:233], v217
	v_smfmac_f32_16x16x64_f16 v[238:241], v[158:161], a[248:255], v210
	ds_read_b128 v[234:237], v217
	s_waitcnt lgkmcnt(5)
	v_smfmac_f32_16x16x64_f16 v[242:245], v[158:161], v[180:187], v210
	s_nop 4
	v_fmac_f32_e32 v238, s40, v239
	s_nop 1
	v_fmac_f32_e32 v242, s40, v243
	v_fmac_f32_e32 v238, s41, v240
	v_fmac_f32_e32 v242, s41, v244
	s_nop 1
	v_permlane32_swap_b32_e32 v238, v242
	v_add_f32_e32 v177, v238, v242
	v_fmac_f32_e32 v198, 0x40638e39, v177
	v_fma_mixlo_f16 v240, v178, v198, v168
	v_fma_f32 v239, v178, v198, v168
	v_fma_mix_f32 v239, v239, 1.0, -v240 op_sel_hi:[0,0,1]
	v_fma_mixlo_f16 v243, v239, s42, 0
	v_fma_mix_f32 v239, v239, s42, -v243 op_sel_hi:[0,0,1]
	v_fma_mixlo_f16 v241, v239, s42, 0
	ds_write_b16 v207, v240
	ds_write_b16 v207, v243 offset:544
	ds_write_b16 v207, v241 offset:1088
	s_waitcnt lgkmcnt(0)
	s_barrier
	ds_read_b128 v[130:133], v208
	ds_read_b128 v[134:137], v209 offset:64
	ds_read_b128 v[138:141], v211
	ds_read_b128 v[142:145], v212
	ds_read_b128 v[146:149], v213
	ds_read_b128 v[150:153], v214
	ds_read_b128 v[154:157], v215
	ds_read_b128 v[158:161], v216
	ds_read_b128 v[180:183], v199 offset:0
	ds_read_b128 v[184:187], v199 offset:1024
	ds_read_b128 v[188:191], v199 offset:4096
	ds_read_b128 v[192:195], v199 offset:5120
	ds_read_b128 v[222:225], v199 offset:8192
	s_waitcnt lgkmcnt(6)
	ds_read_b128 v[226:229], v199 offset:9216
	v_smfmac_f32_16x16x64_f16 v[230:233], v[130:133], a[0:7], v210
	ds_read_b128 v[238:241], v217
	v_smfmac_f32_16x16x64_f16 v[234:237], v[130:133], v[18:25], v210
	ds_read_b128 v[242:245], v217
	v_smfmac_f32_16x16x64_f16 v[230:233], v[134:137], a[40:47], v210
	v_mul_f32_e32 v219, 0x403cf760, v173
	v_smfmac_f32_16x16x64_f16 v[234:237], v[134:137], v[34:41], v210
	v_fmac_f32_e32 v219, 0xc139885f, v162
	v_smfmac_f32_16x16x64_f16 v[230:233], v[138:141], a[64:71], v210
	v_fmac_f32_e32 v219, 0x411d2a92, v166
	v_smfmac_f32_16x16x64_f16 v[234:237], v[138:141], v[42:49], v210
	v_mul_f32_e32 v220, 0x403cf760, v172
	v_smfmac_f32_16x16x64_f16 v[230:233], v[142:145], a[96:103], v210
	v_fmac_f32_e32 v220, 0xc139885f, v163
	v_smfmac_f32_16x16x64_f16 v[234:237], v[142:145], v[58:65], v210
	v_fmac_f32_e32 v220, 0x411d2a92, v167
	v_smfmac_f32_16x16x64_f16 v[230:233], v[146:149], a[128:135], v210
	v_mul_f32_e32 v246, 0x403cf760, v175
	v_smfmac_f32_16x16x64_f16 v[234:237], v[146:149], v[74:81], v210
	v_fmac_f32_e32 v246, 0xc139885f, v164
	v_smfmac_f32_16x16x64_f16 v[230:233], v[150:153], a[160:167], v210
	v_fmac_f32_e32 v246, 0x411d2a92, v176
	v_smfmac_f32_16x16x64_f16 v[234:237], v[150:153], v[98:105], v210
	v_mul_f32_e32 v247, 0x403cf760, v174
	v_smfmac_f32_16x16x64_f16 v[230:233], v[154:157], a[192:199], v210
	v_fmac_f32_e32 v247, 0xc139885f, v165
	v_smfmac_f32_16x16x64_f16 v[234:237], v[154:157], v[106:113], v210
	v_fmac_f32_e32 v247, 0x411d2a92, v177
	s_waitcnt lgkmcnt(8)
	v_smfmac_f32_16x16x64_f16 v[230:233], v[158:161], a[224:231], v210
	v_smfmac_f32_16x16x64_f16 v[234:237], v[158:161], v[122:129], v210
	s_waitcnt lgkmcnt(1)
	v_smfmac_f32_16x16x64_f16 v[238:241], v[130:133], a[16:23], v210
	s_waitcnt lgkmcnt(0)
	v_smfmac_f32_16x16x64_f16 v[242:245], v[130:133], v[180:187], v210
	ds_read_b128 v[180:183], v199 offset:12288
	ds_read_b128 v[184:187], v199 offset:13312
	v_smfmac_f32_16x16x64_f16 v[238:241], v[134:137], a[48:55], v210
	v_fmac_f32_e32 v230, s40, v231
	v_fmac_f32_e32 v234, s40, v235
	v_smfmac_f32_16x16x64_f16 v[242:245], v[134:137], v[188:195], v210
	ds_read_b128 v[188:191], v199 offset:16384
	ds_read_b128 v[192:195], v199 offset:17408
	v_fmac_f32_e32 v230, s41, v232
	v_fmac_f32_e32 v234, s41, v236
	v_smfmac_f32_16x16x64_f16 v[238:241], v[138:141], a[80:87], v210
	s_nop 0
	v_permlane32_swap_b32_e32 v230, v234
	v_add_f32_e32 v179, v230, v234
	v_smfmac_f32_16x16x64_f16 v[242:245], v[138:141], v[222:229], v210
	ds_read_b128 v[222:225], v199 offset:20480
	ds_read_b128 v[226:229], v199 offset:21504
	v_fmac_f32_e32 v219, 0xbe94e4f6, v179
	v_fma_mixlo_f16 v232, v178, v219, v171
	v_smfmac_f32_16x16x64_f16 v[238:241], v[142:145], a[112:119], v210
	v_fma_f32 v231, v178, v219, v171
	v_fma_mix_f32 v231, v231, 1.0, -v232 op_sel_hi:[0,0,1]
	s_waitcnt lgkmcnt(4)
	v_smfmac_f32_16x16x64_f16 v[242:245], v[142:145], v[180:187], v210
	ds_read_b128 v[180:183], v199 offset:24576
	ds_read_b128 v[184:187], v199 offset:25600
	v_fma_mixlo_f16 v235, v231, s42, 0
	v_smfmac_f32_16x16x64_f16 v[238:241], v[146:149], a[144:151], v210
	v_fma_mix_f32 v231, v231, s42, -v235 op_sel_hi:[0,0,1]
	s_waitcnt lgkmcnt(4)
	v_smfmac_f32_16x16x64_f16 v[242:245], v[146:149], v[188:195], v210
	ds_read_b128 v[188:191], v199 offset:28672
	ds_read_b128 v[192:195], v199 offset:29696
	v_fma_mixlo_f16 v233, v231, s42, 0
	v_smfmac_f32_16x16x64_f16 v[238:241], v[150:153], a[176:183], v210
	ds_write_b16 v204, v232 offset:8704
	s_waitcnt lgkmcnt(5)
	v_smfmac_f32_16x16x64_f16 v[242:245], v[150:153], v[222:229], v210
	ds_read_b128 v[222:225], v199 offset:2048
	ds_read_b128 v[226:229], v199 offset:3072
	ds_write_b16 v204, v235 offset:9248
	v_smfmac_f32_16x16x64_f16 v[238:241], v[154:157], a[208:215], v210
	ds_write_b16 v204, v233 offset:9792
	s_waitcnt lgkmcnt(7)
	v_smfmac_f32_16x16x64_f16 v[242:245], v[154:157], v[180:187], v210
	ds_read_b128 v[180:183], v199 offset:6144
	ds_read_b128 v[184:187], v199 offset:7168
	ds_read_b128 v[230:233], v217
	v_smfmac_f32_16x16x64_f16 v[238:241], v[158:161], a[240:247], v210
	ds_read_b128 v[234:237], v217
	s_waitcnt lgkmcnt(9)
	v_smfmac_f32_16x16x64_f16 v[242:245], v[158:161], v[188:195], v210
	ds_read_b128 v[188:191], v199 offset:10240
	ds_read_b128 v[192:195], v199 offset:11264
	s_waitcnt lgkmcnt(3)
	v_smfmac_f32_16x16x64_f16 v[230:233], v[130:133], a[8:15], v210
	s_waitcnt lgkmcnt(2)
	v_smfmac_f32_16x16x64_f16 v[234:237], v[130:133], v[2:9], v210
	v_smfmac_f32_16x16x64_f16 v[230:233], v[134:137], a[32:39], v210
	v_fmac_f32_e32 v238, s40, v239
	v_fmac_f32_e32 v242, s40, v243
	v_smfmac_f32_16x16x64_f16 v[234:237], v[134:137], v[10:17], v210
	v_fmac_f32_e32 v238, s41, v240
	v_fmac_f32_e32 v242, s41, v244
	v_smfmac_f32_16x16x64_f16 v[230:233], v[138:141], a[72:79], v210
	s_nop 0
	v_permlane32_swap_b32_e32 v238, v242
	v_add_f32_e32 v197, v238, v242
	v_smfmac_f32_16x16x64_f16 v[234:237], v[138:141], v[50:57], v210
	v_fmac_f32_e32 v246, 0xbe94e4f6, v197
	v_fma_mixlo_f16 v240, v178, v246, v169
	v_smfmac_f32_16x16x64_f16 v[230:233], v[142:145], a[104:111], v210
	v_fma_f32 v239, v178, v246, v169
	v_fma_mix_f32 v239, v239, 1.0, -v240 op_sel_hi:[0,0,1]
	v_smfmac_f32_16x16x64_f16 v[234:237], v[142:145], v[26:33], v210
	v_fma_mixlo_f16 v243, v239, s42, 0
	v_smfmac_f32_16x16x64_f16 v[230:233], v[146:149], a[136:143], v210
	v_fma_mix_f32 v239, v239, s42, -v243 op_sel_hi:[0,0,1]
	v_smfmac_f32_16x16x64_f16 v[234:237], v[146:149], v[82:89], v210
	v_fma_mixlo_f16 v241, v239, s42, 0
	v_smfmac_f32_16x16x64_f16 v[230:233], v[150:153], a[168:175], v210
	ds_write_b16 v206, v240 offset:8704
	v_smfmac_f32_16x16x64_f16 v[234:237], v[150:153], v[66:73], v210
	ds_write_b16 v206, v243 offset:9248
	v_smfmac_f32_16x16x64_f16 v[230:233], v[154:157], a[200:207], v210
	ds_write_b16 v206, v241 offset:9792
	v_smfmac_f32_16x16x64_f16 v[234:237], v[154:157], v[114:121], v210
	ds_read_b128 v[238:241], v217
	v_smfmac_f32_16x16x64_f16 v[230:233], v[158:161], a[232:239], v210
	ds_read_b128 v[242:245], v217
	v_smfmac_f32_16x16x64_f16 v[234:237], v[158:161], v[90:97], v210
	s_waitcnt lgkmcnt(1)
	v_smfmac_f32_16x16x64_f16 v[238:241], v[130:133], a[24:31], v210
	s_waitcnt lgkmcnt(0)
	v_smfmac_f32_16x16x64_f16 v[242:245], v[130:133], v[222:229], v210
	ds_read_b128 v[222:225], v199 offset:14336
	ds_read_b128 v[226:229], v199 offset:15360
	v_smfmac_f32_16x16x64_f16 v[238:241], v[134:137], a[56:63], v210
	v_fmac_f32_e32 v230, s40, v231
	v_fmac_f32_e32 v234, s40, v235
	v_smfmac_f32_16x16x64_f16 v[242:245], v[134:137], v[180:187], v210
	ds_read_b128 v[180:183], v199 offset:18432
	ds_read_b128 v[184:187], v199 offset:19456
	v_fmac_f32_e32 v230, s41, v232
	v_fmac_f32_e32 v234, s41, v236
	v_smfmac_f32_16x16x64_f16 v[238:241], v[138:141], a[88:95], v210
	s_nop 0
	v_permlane32_swap_b32_e32 v230, v234
	v_add_f32_e32 v196, v230, v234
	v_smfmac_f32_16x16x64_f16 v[242:245], v[138:141], v[188:195], v210
	ds_read_b128 v[188:191], v199 offset:22528
	ds_read_b128 v[192:195], v199 offset:23552
	v_fmac_f32_e32 v220, 0xbe94e4f6, v196
	v_fma_mixlo_f16 v232, v178, v220, v170
	v_smfmac_f32_16x16x64_f16 v[238:241], v[142:145], a[120:127], v210
	v_fma_f32 v231, v178, v220, v170
	v_fma_mix_f32 v231, v231, 1.0, -v232 op_sel_hi:[0,0,1]
	s_waitcnt lgkmcnt(4)
	v_smfmac_f32_16x16x64_f16 v[242:245], v[142:145], v[222:229], v210
	ds_read_b128 v[222:225], v199 offset:26624
	ds_read_b128 v[226:229], v199 offset:27648
	v_fma_mixlo_f16 v235, v231, s42, 0
	v_smfmac_f32_16x16x64_f16 v[238:241], v[146:149], a[152:159], v210
	v_fma_mix_f32 v231, v231, s42, -v235 op_sel_hi:[0,0,1]
	s_waitcnt lgkmcnt(4)
	v_smfmac_f32_16x16x64_f16 v[242:245], v[146:149], v[180:187], v210
	ds_read_b128 v[180:183], v199 offset:30720
	ds_read_b128 v[184:187], v199 offset:31744
	v_fma_mixlo_f16 v233, v231, s42, 0
	v_smfmac_f32_16x16x64_f16 v[238:241], v[150:153], a[184:191], v210
	ds_write_b16 v205, v232 offset:8704
	s_waitcnt lgkmcnt(5)
	v_smfmac_f32_16x16x64_f16 v[242:245], v[150:153], v[188:195], v210
	ds_write_b16 v205, v235 offset:9248
	v_smfmac_f32_16x16x64_f16 v[238:241], v[154:157], a[216:223], v210
	ds_write_b16 v205, v233 offset:9792
	s_waitcnt lgkmcnt(5)
	v_smfmac_f32_16x16x64_f16 v[242:245], v[154:157], v[222:229], v210
	ds_read_b128 v[230:233], v217
	v_smfmac_f32_16x16x64_f16 v[238:241], v[158:161], a[248:255], v210
	ds_read_b128 v[234:237], v217
	s_waitcnt lgkmcnt(5)
	v_smfmac_f32_16x16x64_f16 v[242:245], v[158:161], v[180:187], v210
	s_nop 4
	v_fmac_f32_e32 v238, s40, v239
	s_nop 1
	v_fmac_f32_e32 v242, s40, v243
	v_fmac_f32_e32 v238, s41, v240
	v_fmac_f32_e32 v242, s41, v244
	s_nop 1
	v_permlane32_swap_b32_e32 v238, v242
	v_add_f32_e32 v198, v238, v242
	v_fmac_f32_e32 v247, 0xbe94e4f6, v198
	v_fma_mixlo_f16 v240, v178, v247, v168
	v_fma_f32 v239, v178, v247, v168
	v_fma_mix_f32 v239, v239, 1.0, -v240 op_sel_hi:[0,0,1]
	v_fma_mixlo_f16 v243, v239, s42, 0
	v_fma_mix_f32 v239, v239, s42, -v243 op_sel_hi:[0,0,1]
	v_fma_mixlo_f16 v241, v239, s42, 0
	ds_write_b16 v207, v240 offset:8704
	ds_write_b16 v207, v243 offset:9248
	ds_write_b16 v207, v241 offset:9792
	s_waitcnt lgkmcnt(0)
	s_barrier
	ds_read_b128 v[130:133], v208 offset:8704
	ds_read_b128 v[134:137], v209 offset:8768
	ds_read_b128 v[138:141], v211 offset:8704
	ds_read_b128 v[142:145], v212 offset:8704
	ds_read_b128 v[146:149], v213 offset:8704
	ds_read_b128 v[150:153], v214 offset:8704
	ds_read_b128 v[154:157], v215 offset:8704
	ds_read_b128 v[158:161], v216 offset:8704
	ds_read_b128 v[180:183], v199 offset:0
	ds_read_b128 v[184:187], v199 offset:1024
	ds_read_b128 v[188:191], v199 offset:4096
	ds_read_b128 v[192:195], v199 offset:5120
	ds_read_b128 v[222:225], v199 offset:8192
	s_waitcnt lgkmcnt(6)
	ds_read_b128 v[226:229], v199 offset:9216
	v_smfmac_f32_16x16x64_f16 v[230:233], v[130:133], a[0:7], v210
	ds_read_b128 v[238:241], v217
	ds_read_b128 v[242:245], v217
	v_smfmac_f32_16x16x64_f16 v[234:237], v[130:133], v[18:25], v210
	v_mul_f32_e32 v248, 0x40362960, v173
	v_fmac_f32_e32 v248, 0xc12c1f08, v162
	v_smfmac_f32_16x16x64_f16 v[230:233], v[134:137], a[40:47], v210
	v_fmac_f32_e32 v248, 0x410e80b5, v166
	v_fmac_f32_e32 v248, 0x3e8e8ba3, v179
	v_smfmac_f32_16x16x64_f16 v[234:237], v[134:137], v[34:41], v210
	v_mul_f32_e32 v249, 0x40362960, v172
	v_smfmac_f32_16x16x64_f16 v[230:233], v[138:141], a[64:71], v210
	v_fmac_f32_e32 v249, 0xc12c1f08, v163
	v_smfmac_f32_16x16x64_f16 v[234:237], v[138:141], v[42:49], v210
	v_fmac_f32_e32 v249, 0x410e80b5, v167
	v_smfmac_f32_16x16x64_f16 v[230:233], v[142:145], a[96:103], v210
	v_fmac_f32_e32 v249, 0x3e8e8ba3, v196
	v_smfmac_f32_16x16x64_f16 v[234:237], v[142:145], v[58:65], v210
	v_mul_f32_e32 v250, 0x40362960, v175
	v_smfmac_f32_16x16x64_f16 v[230:233], v[146:149], a[128:135], v210
	v_fmac_f32_e32 v250, 0xc12c1f08, v164
	v_smfmac_f32_16x16x64_f16 v[234:237], v[146:149], v[74:81], v210
	v_fmac_f32_e32 v250, 0x410e80b5, v176
	v_smfmac_f32_16x16x64_f16 v[230:233], v[150:153], a[160:167], v210
	v_fmac_f32_e32 v250, 0x3e8e8ba3, v197
	v_smfmac_f32_16x16x64_f16 v[234:237], v[150:153], v[98:105], v210
	v_mul_f32_e32 v251, 0x40362960, v174
	v_smfmac_f32_16x16x64_f16 v[230:233], v[154:157], a[192:199], v210
	v_fmac_f32_e32 v251, 0xc12c1f08, v165
	v_smfmac_f32_16x16x64_f16 v[234:237], v[154:157], v[106:113], v210
	v_fmac_f32_e32 v251, 0x410e80b5, v177
	s_waitcnt lgkmcnt(8)
	v_smfmac_f32_16x16x64_f16 v[230:233], v[158:161], a[224:231], v210
	v_fmac_f32_e32 v251, 0x3e8e8ba3, v198
	v_smfmac_f32_16x16x64_f16 v[234:237], v[158:161], v[122:129], v210
	s_waitcnt lgkmcnt(1)
	v_smfmac_f32_16x16x64_f16 v[238:241], v[130:133], a[16:23], v210
	s_waitcnt lgkmcnt(0)
	v_smfmac_f32_16x16x64_f16 v[242:245], v[130:133], v[180:187], v210
	ds_read_b128 v[180:183], v199 offset:12288
	ds_read_b128 v[184:187], v199 offset:13312
	v_smfmac_f32_16x16x64_f16 v[238:241], v[134:137], a[48:55], v210
	v_fmac_f32_e32 v230, s40, v231
	v_fmac_f32_e32 v234, s40, v235
	v_smfmac_f32_16x16x64_f16 v[242:245], v[134:137], v[188:195], v210
	ds_read_b128 v[188:191], v199 offset:16384
	ds_read_b128 v[192:195], v199 offset:17408
	v_fmac_f32_e32 v230, s41, v232
	v_fmac_f32_e32 v234, s41, v236
	v_smfmac_f32_16x16x64_f16 v[238:241], v[138:141], a[80:87], v210
	s_nop 0
	v_permlane32_swap_b32_e32 v230, v234
	v_add_f32_e32 v219, v230, v234
	v_smfmac_f32_16x16x64_f16 v[242:245], v[138:141], v[222:229], v210
	ds_read_b128 v[222:225], v199 offset:20480
	ds_read_b128 v[226:229], v199 offset:21504
	v_fmac_f32_e32 v248, 0xbe8c0c4c, v219
	v_fma_mixlo_f16 v232, v178, v248, v171
	v_smfmac_f32_16x16x64_f16 v[238:241], v[142:145], a[112:119], v210
	v_fma_f32 v231, v178, v248, v171
	v_fma_mix_f32 v231, v231, 1.0, -v232 op_sel_hi:[0,0,1]
	s_waitcnt lgkmcnt(4)
	v_smfmac_f32_16x16x64_f16 v[242:245], v[142:145], v[180:187], v210
	ds_read_b128 v[180:183], v199 offset:24576
	ds_read_b128 v[184:187], v199 offset:25600
	v_fma_mixlo_f16 v235, v231, s42, 0
	v_smfmac_f32_16x16x64_f16 v[238:241], v[146:149], a[144:151], v210
	v_fma_mix_f32 v231, v231, s42, -v235 op_sel_hi:[0,0,1]
	s_waitcnt lgkmcnt(4)
	v_smfmac_f32_16x16x64_f16 v[242:245], v[146:149], v[188:195], v210
	ds_read_b128 v[188:191], v199 offset:28672
	ds_read_b128 v[192:195], v199 offset:29696
	v_fma_mixlo_f16 v233, v231, s42, 0
	v_smfmac_f32_16x16x64_f16 v[238:241], v[150:153], a[176:183], v210
	ds_write_b16 v204, v232
	s_waitcnt lgkmcnt(5)
	v_smfmac_f32_16x16x64_f16 v[242:245], v[150:153], v[222:229], v210
	ds_read_b128 v[222:225], v199 offset:2048
	ds_read_b128 v[226:229], v199 offset:3072
	ds_write_b16 v204, v235 offset:544
	v_smfmac_f32_16x16x64_f16 v[238:241], v[154:157], a[208:215], v210
	ds_write_b16 v204, v233 offset:1088
	s_waitcnt lgkmcnt(7)
	v_smfmac_f32_16x16x64_f16 v[242:245], v[154:157], v[180:187], v210
	ds_read_b128 v[180:183], v199 offset:6144
	ds_read_b128 v[184:187], v199 offset:7168
	ds_read_b128 v[230:233], v217
	v_smfmac_f32_16x16x64_f16 v[238:241], v[158:161], a[240:247], v210
	ds_read_b128 v[234:237], v217
	s_waitcnt lgkmcnt(9)
	v_smfmac_f32_16x16x64_f16 v[242:245], v[158:161], v[188:195], v210
	ds_read_b128 v[188:191], v199 offset:10240
	ds_read_b128 v[192:195], v199 offset:11264
	s_waitcnt lgkmcnt(3)
	v_smfmac_f32_16x16x64_f16 v[230:233], v[130:133], a[8:15], v210
	s_waitcnt lgkmcnt(2)
	v_smfmac_f32_16x16x64_f16 v[234:237], v[130:133], v[2:9], v210
	v_smfmac_f32_16x16x64_f16 v[230:233], v[134:137], a[32:39], v210
	v_fmac_f32_e32 v238, s40, v239
	v_fmac_f32_e32 v242, s40, v243
	v_smfmac_f32_16x16x64_f16 v[234:237], v[134:137], v[10:17], v210
	v_fmac_f32_e32 v238, s41, v240
	v_fmac_f32_e32 v242, s41, v244
	v_smfmac_f32_16x16x64_f16 v[230:233], v[138:141], a[72:79], v210
	s_nop 0
	v_permlane32_swap_b32_e32 v238, v242
	v_add_f32_e32 v246, v238, v242
	v_smfmac_f32_16x16x64_f16 v[234:237], v[138:141], v[50:57], v210
	v_fmac_f32_e32 v250, 0xbe8c0c4c, v246
	v_fma_mixlo_f16 v240, v178, v250, v169
	v_smfmac_f32_16x16x64_f16 v[230:233], v[142:145], a[104:111], v210
	v_fma_f32 v239, v178, v250, v169
	v_fma_mix_f32 v239, v239, 1.0, -v240 op_sel_hi:[0,0,1]
	v_smfmac_f32_16x16x64_f16 v[234:237], v[142:145], v[26:33], v210
	v_fma_mixlo_f16 v243, v239, s42, 0
	v_smfmac_f32_16x16x64_f16 v[230:233], v[146:149], a[136:143], v210
	v_fma_mix_f32 v239, v239, s42, -v243 op_sel_hi:[0,0,1]
	v_smfmac_f32_16x16x64_f16 v[234:237], v[146:149], v[82:89], v210
	v_fma_mixlo_f16 v241, v239, s42, 0
	v_smfmac_f32_16x16x64_f16 v[230:233], v[150:153], a[168:175], v210
	ds_write_b16 v206, v240
	v_smfmac_f32_16x16x64_f16 v[234:237], v[150:153], v[66:73], v210
	ds_write_b16 v206, v243 offset:544
	v_smfmac_f32_16x16x64_f16 v[230:233], v[154:157], a[200:207], v210
	ds_write_b16 v206, v241 offset:1088
	v_smfmac_f32_16x16x64_f16 v[234:237], v[154:157], v[114:121], v210
	ds_read_b128 v[238:241], v217
	v_smfmac_f32_16x16x64_f16 v[230:233], v[158:161], a[232:239], v210
	ds_read_b128 v[242:245], v217
	v_smfmac_f32_16x16x64_f16 v[234:237], v[158:161], v[90:97], v210
	s_waitcnt lgkmcnt(1)
	v_smfmac_f32_16x16x64_f16 v[238:241], v[130:133], a[24:31], v210
	s_waitcnt lgkmcnt(0)
	v_smfmac_f32_16x16x64_f16 v[242:245], v[130:133], v[222:229], v210
	ds_read_b128 v[222:225], v199 offset:14336
	ds_read_b128 v[226:229], v199 offset:15360
	v_smfmac_f32_16x16x64_f16 v[238:241], v[134:137], a[56:63], v210
	v_fmac_f32_e32 v230, s40, v231
	v_fmac_f32_e32 v234, s40, v235
	v_smfmac_f32_16x16x64_f16 v[242:245], v[134:137], v[180:187], v210
	ds_read_b128 v[180:183], v199 offset:18432
	ds_read_b128 v[184:187], v199 offset:19456
	v_fmac_f32_e32 v230, s41, v232
	v_fmac_f32_e32 v234, s41, v236
	v_smfmac_f32_16x16x64_f16 v[238:241], v[138:141], a[88:95], v210
	s_nop 0
	v_permlane32_swap_b32_e32 v230, v234
	v_add_f32_e32 v220, v230, v234
	v_smfmac_f32_16x16x64_f16 v[242:245], v[138:141], v[188:195], v210
	ds_read_b128 v[188:191], v199 offset:22528
	ds_read_b128 v[192:195], v199 offset:23552
	v_fmac_f32_e32 v249, 0xbe8c0c4c, v220
	v_fma_mixlo_f16 v232, v178, v249, v170
	v_smfmac_f32_16x16x64_f16 v[238:241], v[142:145], a[120:127], v210
	v_fma_f32 v231, v178, v249, v170
	v_fma_mix_f32 v231, v231, 1.0, -v232 op_sel_hi:[0,0,1]
	s_waitcnt lgkmcnt(4)
	v_smfmac_f32_16x16x64_f16 v[242:245], v[142:145], v[222:229], v210
	ds_read_b128 v[222:225], v199 offset:26624
	ds_read_b128 v[226:229], v199 offset:27648
	v_fma_mixlo_f16 v235, v231, s42, 0
	v_smfmac_f32_16x16x64_f16 v[238:241], v[146:149], a[152:159], v210
	v_fma_mix_f32 v231, v231, s42, -v235 op_sel_hi:[0,0,1]
	s_waitcnt lgkmcnt(4)
	v_smfmac_f32_16x16x64_f16 v[242:245], v[146:149], v[180:187], v210
	ds_read_b128 v[180:183], v199 offset:30720
	ds_read_b128 v[184:187], v199 offset:31744
	v_fma_mixlo_f16 v233, v231, s42, 0
	v_smfmac_f32_16x16x64_f16 v[238:241], v[150:153], a[184:191], v210
	ds_write_b16 v205, v232
	s_waitcnt lgkmcnt(5)
	v_smfmac_f32_16x16x64_f16 v[242:245], v[150:153], v[188:195], v210
	ds_write_b16 v205, v235 offset:544
	v_smfmac_f32_16x16x64_f16 v[238:241], v[154:157], a[216:223], v210
	ds_write_b16 v205, v233 offset:1088
	s_waitcnt lgkmcnt(5)
	v_smfmac_f32_16x16x64_f16 v[242:245], v[154:157], v[222:229], v210
	ds_read_b128 v[230:233], v217
	v_smfmac_f32_16x16x64_f16 v[238:241], v[158:161], a[248:255], v210
	ds_read_b128 v[234:237], v217
	s_waitcnt lgkmcnt(5)
	v_smfmac_f32_16x16x64_f16 v[242:245], v[158:161], v[180:187], v210
	s_nop 4
	v_fmac_f32_e32 v238, s40, v239
	s_nop 1
	v_fmac_f32_e32 v242, s40, v243
	v_fmac_f32_e32 v238, s41, v240
	v_fmac_f32_e32 v242, s41, v244
	s_nop 1
	v_permlane32_swap_b32_e32 v238, v242
	v_add_f32_e32 v247, v238, v242
	v_fmac_f32_e32 v251, 0xbe8c0c4c, v247
	v_fma_mixlo_f16 v240, v178, v251, v168
	v_fma_f32 v239, v178, v251, v168
	v_fma_mix_f32 v239, v239, 1.0, -v240 op_sel_hi:[0,0,1]
	v_fma_mixlo_f16 v243, v239, s42, 0
	v_fma_mix_f32 v239, v239, s42, -v243 op_sel_hi:[0,0,1]
	v_fma_mixlo_f16 v241, v239, s42, 0
	ds_write_b16 v207, v240
	ds_write_b16 v207, v243 offset:544
	ds_write_b16 v207, v241 offset:1088
	s_waitcnt lgkmcnt(0)
	s_barrier
	ds_read_b128 v[130:133], v208
	ds_read_b128 v[134:137], v209 offset:64
	ds_read_b128 v[138:141], v211
	ds_read_b128 v[142:145], v212
	ds_read_b128 v[146:149], v213
	ds_read_b128 v[150:153], v214
	ds_read_b128 v[154:157], v215
	ds_read_b128 v[158:161], v216
	ds_read_b128 v[180:183], v199 offset:0
	ds_read_b128 v[184:187], v199 offset:1024
	ds_read_b128 v[188:191], v199 offset:4096
	ds_read_b128 v[192:195], v199 offset:5120
	ds_read_b128 v[222:225], v199 offset:8192
	s_waitcnt lgkmcnt(6)
	ds_read_b128 v[226:229], v199 offset:9216
	v_smfmac_f32_16x16x64_f16 v[230:233], v[130:133], a[0:7], v210
	ds_read_b128 v[238:241], v217
	ds_read_b128 v[242:245], v217
	v_smfmac_f32_16x16x64_f16 v[234:237], v[130:133], v[18:25], v210
	v_mul_f32_e32 v252, 0x3dbaaaab, v173
	v_fmac_f32_e32 v252, 0x3ee6024d, v166
	v_smfmac_f32_16x16x64_f16 v[230:233], v[134:137], a[40:47], v210
	v_fmac_f32_e32 v252, 0x3f26aaab, v179
	v_fmac_f32_e32 v252, 0xbea50e7e, v219
	v_smfmac_f32_16x16x64_f16 v[234:237], v[134:137], v[34:41], v210
	v_mul_f32_e32 v253, 0x3dbaaaab, v172
	v_smfmac_f32_16x16x64_f16 v[230:233], v[138:141], a[64:71], v210
	v_fmac_f32_e32 v253, 0x3ee6024d, v167
	v_smfmac_f32_16x16x64_f16 v[234:237], v[138:141], v[42:49], v210
	v_fmac_f32_e32 v253, 0x3f26aaab, v196
	v_smfmac_f32_16x16x64_f16 v[230:233], v[142:145], a[96:103], v210
	v_fmac_f32_e32 v253, 0xbea50e7e, v220
	v_smfmac_f32_16x16x64_f16 v[234:237], v[142:145], v[58:65], v210
	v_mul_f32_e32 v254, 0x3dbaaaab, v175
	v_smfmac_f32_16x16x64_f16 v[230:233], v[146:149], a[128:135], v210
	v_fmac_f32_e32 v254, 0x3ee6024d, v176
	v_smfmac_f32_16x16x64_f16 v[234:237], v[146:149], v[74:81], v210
	v_fmac_f32_e32 v254, 0x3f26aaab, v197
	v_smfmac_f32_16x16x64_f16 v[230:233], v[150:153], a[160:167], v210
	v_fmac_f32_e32 v254, 0xbea50e7e, v246
	v_smfmac_f32_16x16x64_f16 v[234:237], v[150:153], v[98:105], v210
	v_mul_f32_e32 v255, 0x3dbaaaab, v174
	v_smfmac_f32_16x16x64_f16 v[230:233], v[154:157], a[192:199], v210
	v_fmac_f32_e32 v255, 0x3ee6024d, v177
	v_smfmac_f32_16x16x64_f16 v[234:237], v[154:157], v[106:113], v210
	v_fmac_f32_e32 v255, 0x3f26aaab, v198
	s_waitcnt lgkmcnt(8)
	v_smfmac_f32_16x16x64_f16 v[230:233], v[158:161], a[224:231], v210
	v_fmac_f32_e32 v255, 0xbea50e7e, v247
	v_smfmac_f32_16x16x64_f16 v[234:237], v[158:161], v[122:129], v210
	s_waitcnt lgkmcnt(1)
	v_smfmac_f32_16x16x64_f16 v[238:241], v[130:133], a[16:23], v210
	s_waitcnt lgkmcnt(0)
	v_smfmac_f32_16x16x64_f16 v[242:245], v[130:133], v[180:187], v210
	ds_read_b128 v[180:183], v199 offset:12288
	ds_read_b128 v[184:187], v199 offset:13312
	v_smfmac_f32_16x16x64_f16 v[238:241], v[134:137], a[48:55], v210
	v_fmac_f32_e32 v230, s40, v231
	v_fmac_f32_e32 v234, s40, v235
	v_smfmac_f32_16x16x64_f16 v[242:245], v[134:137], v[188:195], v210
	ds_read_b128 v[188:191], v199 offset:16384
	ds_read_b128 v[192:195], v199 offset:17408
	v_fmac_f32_e32 v230, s41, v232
	v_fmac_f32_e32 v234, s41, v236
	v_smfmac_f32_16x16x64_f16 v[238:241], v[138:141], a[80:87], v210
	s_nop 0
	v_permlane32_swap_b32_e32 v230, v234
	v_add_f32_e32 v248, v230, v234
	v_smfmac_f32_16x16x64_f16 v[242:245], v[138:141], v[222:229], v210
	ds_read_b128 v[222:225], v199 offset:20480
	ds_read_b128 v[226:229], v199 offset:21504
	v_fmac_f32_e32 v252, 0x3e061862, v248
	v_mov_b32_e32 v236, v252
	v_smfmac_f32_16x16x64_f16 v[238:241], v[142:145], a[112:119], v210
	v_fma_mixlo_f16 v232, v178, v236, v171
	v_fma_f32 v252, v178, v236, v171
	s_waitcnt lgkmcnt(4)
	v_smfmac_f32_16x16x64_f16 v[242:245], v[142:145], v[180:187], v210
	ds_read_b128 v[180:183], v199 offset:24576
	ds_read_b128 v[184:187], v199 offset:25600
	v_fma_mix_f32 v231, v252, 1.0, -v232 op_sel_hi:[0,0,1]
	v_fma_mixlo_f16 v235, v231, s42, 0
	v_smfmac_f32_16x16x64_f16 v[238:241], v[146:149], a[144:151], v210
	v_fma_mix_f32 v231, v231, s42, -v235 op_sel_hi:[0,0,1]
	s_waitcnt lgkmcnt(4)
	v_smfmac_f32_16x16x64_f16 v[242:245], v[146:149], v[188:195], v210
	ds_read_b128 v[188:191], v199 offset:28672
	ds_read_b128 v[192:195], v199 offset:29696
	v_fma_mixlo_f16 v233, v231, s42, 0
	v_smfmac_f32_16x16x64_f16 v[238:241], v[150:153], a[176:183], v210
	ds_write_b16 v204, v232 offset:8704
	s_waitcnt lgkmcnt(5)
	v_smfmac_f32_16x16x64_f16 v[242:245], v[150:153], v[222:229], v210
	ds_read_b128 v[222:225], v199 offset:2048
	ds_read_b128 v[226:229], v199 offset:3072
	ds_write_b16 v204, v235 offset:9248
	v_smfmac_f32_16x16x64_f16 v[238:241], v[154:157], a[208:215], v210
	ds_write_b16 v204, v233 offset:9792
	s_waitcnt lgkmcnt(7)
	v_smfmac_f32_16x16x64_f16 v[242:245], v[154:157], v[180:187], v210
	ds_read_b128 v[180:183], v199 offset:6144
	ds_read_b128 v[184:187], v199 offset:7168
	ds_read_b128 v[230:233], v217
	v_smfmac_f32_16x16x64_f16 v[238:241], v[158:161], a[240:247], v210
	ds_read_b128 v[234:237], v217
	s_waitcnt lgkmcnt(9)
	v_smfmac_f32_16x16x64_f16 v[242:245], v[158:161], v[188:195], v210
	ds_read_b128 v[188:191], v199 offset:10240
	ds_read_b128 v[192:195], v199 offset:11264
	s_waitcnt lgkmcnt(3)
	v_smfmac_f32_16x16x64_f16 v[230:233], v[130:133], a[8:15], v210
	s_waitcnt lgkmcnt(2)
	v_smfmac_f32_16x16x64_f16 v[234:237], v[130:133], v[2:9], v210
	v_smfmac_f32_16x16x64_f16 v[230:233], v[134:137], a[32:39], v210
	v_fmac_f32_e32 v238, s40, v239
	v_fmac_f32_e32 v242, s40, v243
	v_smfmac_f32_16x16x64_f16 v[234:237], v[134:137], v[10:17], v210
	v_fmac_f32_e32 v238, s41, v240
	v_fmac_f32_e32 v242, s41, v244
	v_smfmac_f32_16x16x64_f16 v[230:233], v[138:141], a[72:79], v210
	s_nop 0
	v_permlane32_swap_b32_e32 v238, v242
	v_add_f32_e32 v250, v238, v242
	v_smfmac_f32_16x16x64_f16 v[234:237], v[138:141], v[50:57], v210
	v_fmac_f32_e32 v254, 0x3e061862, v250
	v_mov_b32_e32 v244, v254
	v_smfmac_f32_16x16x64_f16 v[230:233], v[142:145], a[104:111], v210
	v_fma_mixlo_f16 v240, v178, v244, v169
	v_fma_f32 v254, v178, v244, v169
	v_smfmac_f32_16x16x64_f16 v[234:237], v[142:145], v[26:33], v210
	v_fma_mix_f32 v239, v254, 1.0, -v240 op_sel_hi:[0,0,1]
	v_fma_mixlo_f16 v243, v239, s42, 0
	v_smfmac_f32_16x16x64_f16 v[230:233], v[146:149], a[136:143], v210
	v_fma_mix_f32 v239, v239, s42, -v243 op_sel_hi:[0,0,1]
	v_smfmac_f32_16x16x64_f16 v[234:237], v[146:149], v[82:89], v210
	v_fma_mixlo_f16 v241, v239, s42, 0
	v_smfmac_f32_16x16x64_f16 v[230:233], v[150:153], a[168:175], v210
	ds_write_b16 v206, v240 offset:8704
	v_smfmac_f32_16x16x64_f16 v[234:237], v[150:153], v[66:73], v210
	ds_write_b16 v206, v243 offset:9248
	v_smfmac_f32_16x16x64_f16 v[230:233], v[154:157], a[200:207], v210
	ds_write_b16 v206, v241 offset:9792
	v_smfmac_f32_16x16x64_f16 v[234:237], v[154:157], v[114:121], v210
	ds_read_b128 v[238:241], v217
	v_smfmac_f32_16x16x64_f16 v[230:233], v[158:161], a[232:239], v210
	ds_read_b128 v[242:245], v217
	v_smfmac_f32_16x16x64_f16 v[234:237], v[158:161], v[90:97], v210
	s_waitcnt lgkmcnt(1)
	v_smfmac_f32_16x16x64_f16 v[238:241], v[130:133], a[24:31], v210
	s_waitcnt lgkmcnt(0)
	v_smfmac_f32_16x16x64_f16 v[242:245], v[130:133], v[222:229], v210
	ds_read_b128 v[222:225], v199 offset:14336
	ds_read_b128 v[226:229], v199 offset:15360
	v_smfmac_f32_16x16x64_f16 v[238:241], v[134:137], a[56:63], v210
	v_fmac_f32_e32 v230, s40, v231
	v_fmac_f32_e32 v234, s40, v235
	v_smfmac_f32_16x16x64_f16 v[242:245], v[134:137], v[180:187], v210
	ds_read_b128 v[180:183], v199 offset:18432
	ds_read_b128 v[184:187], v199 offset:19456
	v_fmac_f32_e32 v230, s41, v232
	v_fmac_f32_e32 v234, s41, v236
	v_smfmac_f32_16x16x64_f16 v[238:241], v[138:141], a[88:95], v210
	s_nop 0
	v_permlane32_swap_b32_e32 v230, v234
	v_add_f32_e32 v249, v230, v234
	v_smfmac_f32_16x16x64_f16 v[242:245], v[138:141], v[188:195], v210
	ds_read_b128 v[188:191], v199 offset:22528
	ds_read_b128 v[192:195], v199 offset:23552
	v_fmac_f32_e32 v253, 0x3e061862, v249
	v_mov_b32_e32 v236, v253
	v_smfmac_f32_16x16x64_f16 v[238:241], v[142:145], a[120:127], v210
	v_fma_mixlo_f16 v232, v178, v236, v170
	v_fma_f32 v253, v178, v236, v170
	s_waitcnt lgkmcnt(4)
	v_smfmac_f32_16x16x64_f16 v[242:245], v[142:145], v[222:229], v210
	ds_read_b128 v[222:225], v199 offset:26624
	ds_read_b128 v[226:229], v199 offset:27648
	v_fma_mix_f32 v231, v253, 1.0, -v232 op_sel_hi:[0,0,1]
	v_fma_mixlo_f16 v235, v231, s42, 0
	v_smfmac_f32_16x16x64_f16 v[238:241], v[146:149], a[152:159], v210
	v_fma_mix_f32 v231, v231, s42, -v235 op_sel_hi:[0,0,1]
	s_waitcnt lgkmcnt(4)
	v_smfmac_f32_16x16x64_f16 v[242:245], v[146:149], v[180:187], v210
	ds_read_b128 v[180:183], v199 offset:30720
	ds_read_b128 v[184:187], v199 offset:31744
	v_fma_mixlo_f16 v233, v231, s42, 0
	v_smfmac_f32_16x16x64_f16 v[238:241], v[150:153], a[184:191], v210
	ds_write_b16 v205, v232 offset:8704
	s_waitcnt lgkmcnt(5)
	v_smfmac_f32_16x16x64_f16 v[242:245], v[150:153], v[188:195], v210
	ds_write_b16 v205, v235 offset:9248
	v_smfmac_f32_16x16x64_f16 v[238:241], v[154:157], a[216:223], v210
	ds_write_b16 v205, v233 offset:9792
	s_waitcnt lgkmcnt(5)
	v_smfmac_f32_16x16x64_f16 v[242:245], v[154:157], v[222:229], v210
	ds_read_b128 v[230:233], v217
	v_smfmac_f32_16x16x64_f16 v[238:241], v[158:161], a[248:255], v210
	ds_read_b128 v[234:237], v217
	s_waitcnt lgkmcnt(5)
	v_smfmac_f32_16x16x64_f16 v[242:245], v[158:161], v[180:187], v210
	s_nop 4
	v_fmac_f32_e32 v238, s40, v239
	s_nop 1
	v_fmac_f32_e32 v242, s40, v243
	v_fmac_f32_e32 v238, s41, v240
	v_fmac_f32_e32 v242, s41, v244
	s_nop 1
	v_permlane32_swap_b32_e32 v238, v242
	v_add_f32_e32 v251, v238, v242
	v_fmac_f32_e32 v255, 0x3e061862, v251
	v_mov_b32_e32 v244, v255
	v_fma_mixlo_f16 v240, v178, v244, v168
	v_fma_f32 v255, v178, v244, v168
	v_fma_mix_f32 v239, v255, 1.0, -v240 op_sel_hi:[0,0,1]
	v_fma_mixlo_f16 v243, v239, s42, 0
	v_fma_mix_f32 v239, v239, s42, -v243 op_sel_hi:[0,0,1]
	v_fma_mixlo_f16 v241, v239, s42, 0
	ds_write_b16 v207, v240 offset:8704
	ds_write_b16 v207, v243 offset:9248
	ds_write_b16 v207, v241 offset:9792
	s_waitcnt lgkmcnt(0)
	s_barrier
	ds_read_b128 v[130:133], v208 offset:8704
	ds_read_b128 v[134:137], v209 offset:8768
	ds_read_b128 v[138:141], v211 offset:8704
	ds_read_b128 v[142:145], v212 offset:8704
	ds_read_b128 v[146:149], v213 offset:8704
	ds_read_b128 v[150:153], v214 offset:8704
	ds_read_b128 v[154:157], v215 offset:8704
	ds_read_b128 v[158:161], v216 offset:8704
	ds_read_b128 v[180:183], v199 offset:0
	ds_read_b128 v[184:187], v199 offset:1024
	ds_read_b128 v[188:191], v199 offset:4096
	ds_read_b128 v[192:195], v199 offset:5120
	ds_read_b128 v[222:225], v199 offset:8192
	s_waitcnt lgkmcnt(6)
	ds_read_b128 v[226:229], v199 offset:9216
	v_smfmac_f32_16x16x64_f16 v[230:233], v[130:133], a[0:7], v210
	ds_read_b128 v[238:241], v217
	ds_read_b128 v[242:245], v217
	v_smfmac_f32_16x16x64_f16 v[234:237], v[130:133], v[18:25], v210
	v_mul_f32_e32 v162, 0x3aa1907f, v173
	v_fmac_f32_e32 v162, 0xbb8b5ad3, v166
	v_smfmac_f32_16x16x64_f16 v[230:233], v[134:137], a[40:47], v210
	v_fmac_f32_e32 v162, 0x3d177777, v179
	v_fmac_f32_e32 v162, 0xbd50568f, v219
	v_smfmac_f32_16x16x64_f16 v[234:237], v[134:137], v[34:41], v210
	v_fmac_f32_e32 v162, 0x3d2ba454, v248
	v_mul_f32_e32 v163, 0x3aa1907f, v172
	v_smfmac_f32_16x16x64_f16 v[230:233], v[138:141], a[64:71], v210
	v_fmac_f32_e32 v163, 0xbb8b5ad3, v167
	v_fmac_f32_e32 v163, 0x3d177777, v196
	v_smfmac_f32_16x16x64_f16 v[234:237], v[138:141], v[42:49], v210
	v_fmac_f32_e32 v163, 0xbd50568f, v220
	v_fmac_f32_e32 v163, 0x3d2ba454, v249
	v_smfmac_f32_16x16x64_f16 v[230:233], v[142:145], a[96:103], v210
	v_mul_f32_e32 v164, 0x3aa1907f, v175
	v_fmac_f32_e32 v164, 0xbb8b5ad3, v176
	v_smfmac_f32_16x16x64_f16 v[234:237], v[142:145], v[58:65], v210
	v_fmac_f32_e32 v164, 0x3d177777, v197
	v_fmac_f32_e32 v164, 0xbd50568f, v246
	v_smfmac_f32_16x16x64_f16 v[230:233], v[146:149], a[128:135], v210
	v_fmac_f32_e32 v164, 0x3d2ba454, v250
	v_mul_f32_e32 v165, 0x3aa1907f, v174
	v_smfmac_f32_16x16x64_f16 v[234:237], v[146:149], v[74:81], v210
	v_fmac_f32_e32 v165, 0xbb8b5ad3, v177
	v_fmac_f32_e32 v165, 0x3d177777, v198
	v_smfmac_f32_16x16x64_f16 v[230:233], v[150:153], a[160:167], v210
	v_fmac_f32_e32 v165, 0xbd50568f, v247
	v_fmac_f32_e32 v165, 0x3d2ba454, v251
	v_smfmac_f32_16x16x64_f16 v[234:237], v[150:153], v[98:105], v210
	v_max_f32_e64 v179, |v171|, |v252|
	v_mov_b32_e32 v248, 0x358637bd
	v_smfmac_f32_16x16x64_f16 v[230:233], v[154:157], a[192:199], v210
	v_fmac_f32_e32 v248, 0x3a83126f, v179
	v_rcp_f32_e32 v179, v248
	v_smfmac_f32_16x16x64_f16 v[234:237], v[154:157], v[106:113], v210
	v_max_f32_e64 v196, |v170|, |v253|
	v_mov_b32_e32 v249, 0x358637bd
	s_waitcnt lgkmcnt(8)
	v_smfmac_f32_16x16x64_f16 v[230:233], v[158:161], a[224:231], v210
	v_fmac_f32_e32 v249, 0x3a83126f, v196
	v_rcp_f32_e32 v196, v249
	v_smfmac_f32_16x16x64_f16 v[234:237], v[158:161], v[122:129], v210
	v_max_f32_e64 v197, |v169|, |v254|
	v_mov_b32_e32 v250, 0x358637bd
	v_fmac_f32_e32 v250, 0x3a83126f, v197
	v_rcp_f32_e32 v197, v250
	v_max_f32_e64 v198, |v168|, |v255|
	v_mov_b32_e32 v251, 0x358637bd
	v_fmac_f32_e32 v251, 0x3a83126f, v198
	v_rcp_f32_e32 v198, v251
	s_waitcnt lgkmcnt(1)
	v_smfmac_f32_16x16x64_f16 v[238:241], v[130:133], a[16:23], v210
	s_waitcnt lgkmcnt(0)
	v_smfmac_f32_16x16x64_f16 v[242:245], v[130:133], v[180:187], v210
	ds_read_b128 v[180:183], v199 offset:12288
	ds_read_b128 v[184:187], v199 offset:13312
	v_smfmac_f32_16x16x64_f16 v[238:241], v[134:137], a[48:55], v210
	v_fmac_f32_e32 v230, s40, v231
	v_smfmac_f32_16x16x64_f16 v[242:245], v[134:137], v[188:195], v210
	ds_read_b128 v[188:191], v199 offset:16384
	ds_read_b128 v[192:195], v199 offset:17408
	v_fmac_f32_e32 v234, s40, v235
	v_smfmac_f32_16x16x64_f16 v[238:241], v[138:141], a[80:87], v210
	v_fmac_f32_e32 v230, s41, v232
	v_smfmac_f32_16x16x64_f16 v[242:245], v[138:141], v[222:229], v210
	ds_read_b128 v[222:225], v199 offset:20480
	ds_read_b128 v[226:229], v199 offset:21504
	v_fmac_f32_e32 v234, s41, v236
	v_smfmac_f32_16x16x64_f16 v[238:241], v[142:145], a[112:119], v210
	s_nop 0
	v_permlane32_swap_b32_e32 v230, v234
	s_waitcnt lgkmcnt(4)
	v_smfmac_f32_16x16x64_f16 v[242:245], v[142:145], v[180:187], v210
	ds_read_b128 v[180:183], v199 offset:24576
	ds_read_b128 v[184:187], v199 offset:25600
	v_add_f32_e32 v166, v230, v234
	v_smfmac_f32_16x16x64_f16 v[238:241], v[146:149], a[144:151], v210
	v_fmac_f32_e32 v162, 0xbccccccd, v166
	s_waitcnt lgkmcnt(4)
	v_smfmac_f32_16x16x64_f16 v[242:245], v[146:149], v[188:195], v210
	ds_read_b128 v[188:191], v199 offset:28672
	ds_read_b128 v[192:195], v199 offset:29696
	v_mul_f32_e32 v231, v178, v162
	v_smfmac_f32_16x16x64_f16 v[238:241], v[150:153], a[176:183], v210
	v_mul_f32_e32 v231, v231, v179
	s_waitcnt lgkmcnt(4)
	v_smfmac_f32_16x16x64_f16 v[242:245], v[150:153], v[222:229], v210
	ds_read_b128 v[222:225], v199 offset:2048
	ds_read_b128 v[226:229], v199 offset:3072
	v_mul_f32_e32 v219, v231, v231
	v_smfmac_f32_16x16x64_f16 v[238:241], v[154:157], a[208:215], v210
	ds_read_b128 v[230:233], v217
	s_waitcnt lgkmcnt(5)
	v_smfmac_f32_16x16x64_f16 v[242:245], v[154:157], v[180:187], v210
	ds_read_b128 v[180:183], v199 offset:6144
	ds_read_b128 v[184:187], v199 offset:7168
	ds_read_b128 v[234:237], v217
	v_smfmac_f32_16x16x64_f16 v[238:241], v[158:161], a[240:247], v210
	s_waitcnt lgkmcnt(6)
	v_smfmac_f32_16x16x64_f16 v[242:245], v[158:161], v[188:195], v210
	ds_read_b128 v[188:191], v199 offset:10240
	ds_read_b128 v[192:195], v199 offset:11264
	s_waitcnt lgkmcnt(5)
	v_smfmac_f32_16x16x64_f16 v[230:233], v[130:133], a[8:15], v210
	s_waitcnt lgkmcnt(2)
	v_smfmac_f32_16x16x64_f16 v[234:237], v[130:133], v[2:9], v210
	v_smfmac_f32_16x16x64_f16 v[230:233], v[134:137], a[32:39], v210
	v_fmac_f32_e32 v238, s40, v239
	v_smfmac_f32_16x16x64_f16 v[234:237], v[134:137], v[10:17], v210
	v_fmac_f32_e32 v242, s40, v243
	v_smfmac_f32_16x16x64_f16 v[230:233], v[138:141], a[72:79], v210
	v_fmac_f32_e32 v238, s41, v240
	v_smfmac_f32_16x16x64_f16 v[234:237], v[138:141], v[50:57], v210
	v_fmac_f32_e32 v242, s41, v244
	v_smfmac_f32_16x16x64_f16 v[230:233], v[142:145], a[104:111], v210
	s_nop 0
	v_permlane32_swap_b32_e32 v238, v242
	v_smfmac_f32_16x16x64_f16 v[234:237], v[142:145], v[26:33], v210
	v_add_f32_e32 v176, v238, v242
	v_smfmac_f32_16x16x64_f16 v[230:233], v[146:149], a[136:143], v210
	v_fmac_f32_e32 v164, 0xbccccccd, v176
	v_smfmac_f32_16x16x64_f16 v[234:237], v[146:149], v[82:89], v210
	v_mul_f32_e32 v239, v178, v164
	v_smfmac_f32_16x16x64_f16 v[230:233], v[150:153], a[168:175], v210
	v_mul_f32_e32 v239, v239, v197
	v_smfmac_f32_16x16x64_f16 v[234:237], v[150:153], v[66:73], v210
	v_fmac_f32_e32 v219, v239, v239
	v_smfmac_f32_16x16x64_f16 v[230:233], v[154:157], a[200:207], v210
	ds_read_b128 v[238:241], v217
	v_smfmac_f32_16x16x64_f16 v[234:237], v[154:157], v[114:121], v210
	ds_read_b128 v[242:245], v217
	v_smfmac_f32_16x16x64_f16 v[230:233], v[158:161], a[232:239], v210
	v_smfmac_f32_16x16x64_f16 v[234:237], v[158:161], v[90:97], v210
	s_waitcnt lgkmcnt(1)
	v_smfmac_f32_16x16x64_f16 v[238:241], v[130:133], a[24:31], v210
	s_waitcnt lgkmcnt(0)
	v_smfmac_f32_16x16x64_f16 v[242:245], v[130:133], v[222:229], v210
	ds_read_b128 v[222:225], v199 offset:14336
	ds_read_b128 v[226:229], v199 offset:15360
	v_smfmac_f32_16x16x64_f16 v[238:241], v[134:137], a[56:63], v210
	v_fmac_f32_e32 v230, s40, v231
	v_smfmac_f32_16x16x64_f16 v[242:245], v[134:137], v[180:187], v210
	ds_read_b128 v[180:183], v199 offset:18432
	ds_read_b128 v[184:187], v199 offset:19456
	v_fmac_f32_e32 v234, s40, v235
	v_smfmac_f32_16x16x64_f16 v[238:241], v[138:141], a[88:95], v210
	v_fmac_f32_e32 v230, s41, v232
	v_smfmac_f32_16x16x64_f16 v[242:245], v[138:141], v[188:195], v210
	ds_read_b128 v[188:191], v199 offset:22528
	ds_read_b128 v[192:195], v199 offset:23552
	v_fmac_f32_e32 v234, s41, v236
	v_smfmac_f32_16x16x64_f16 v[238:241], v[142:145], a[120:127], v210
	s_nop 0
	v_permlane32_swap_b32_e32 v230, v234
	s_waitcnt lgkmcnt(4)
	v_smfmac_f32_16x16x64_f16 v[242:245], v[142:145], v[222:229], v210
	ds_read_b128 v[222:225], v199 offset:26624
	ds_read_b128 v[226:229], v199 offset:27648
	v_add_f32_e32 v167, v230, v234
	v_smfmac_f32_16x16x64_f16 v[238:241], v[146:149], a[152:159], v210
	v_fmac_f32_e32 v163, 0xbccccccd, v167
	s_waitcnt lgkmcnt(4)
	v_smfmac_f32_16x16x64_f16 v[242:245], v[146:149], v[180:187], v210
	ds_read_b128 v[180:183], v199 offset:30720
	ds_read_b128 v[184:187], v199 offset:31744
	v_mul_f32_e32 v231, v178, v163
	v_smfmac_f32_16x16x64_f16 v[238:241], v[150:153], a[184:191], v210
	v_mul_f32_e32 v231, v231, v196
	s_waitcnt lgkmcnt(4)
	v_smfmac_f32_16x16x64_f16 v[242:245], v[150:153], v[188:195], v210
	v_fmac_f32_e32 v219, v231, v231
	v_smfmac_f32_16x16x64_f16 v[238:241], v[154:157], a[216:223], v210
	ds_read_b128 v[230:233], v217
	s_waitcnt lgkmcnt(3)
	v_smfmac_f32_16x16x64_f16 v[242:245], v[154:157], v[222:229], v210
	ds_read_b128 v[234:237], v217
	v_smfmac_f32_16x16x64_f16 v[238:241], v[158:161], a[248:255], v210
	s_waitcnt lgkmcnt(2)
	v_smfmac_f32_16x16x64_f16 v[242:245], v[158:161], v[180:187], v210
	s_nop 5
	v_fmac_f32_e32 v238, s40, v239
	s_nop 0
	v_fmac_f32_e32 v242, s40, v243
	v_fmac_f32_e32 v238, s41, v240
	v_fmac_f32_e32 v242, s41, v244
	s_nop 1
	v_permlane32_swap_b32_e32 v238, v242
	v_add_f32_e32 v177, v238, v242
	v_fmac_f32_e32 v165, 0xbccccccd, v177
	v_mul_f32_e32 v239, v178, v165
	v_mul_f32_e32 v239, v239, v198
	v_fmac_f32_e32 v219, v239, v239
	s_nop 1
	v_add_f32_dpp v238, v219, v219 quad_perm:[1,0,3,2] row_mask:0xf bank_mask:0xf bound_ctrl:1
	s_nop 1
	v_add_f32_dpp v238, v238, v238 quad_perm:[2,3,0,1] row_mask:0xf bank_mask:0xf bound_ctrl:1
	s_nop 1
	v_add_f32_dpp v238, v238, v238 row_half_mirror row_mask:0xf bank_mask:0xf bound_ctrl:1
	s_nop 1
	v_add_f32_dpp v238, v238, v238 row_mirror row_mask:0xf bank_mask:0xf bound_ctrl:1
	v_mov_b32_e32 v239, v238
	s_nop 1
	v_permlane32_swap_b32_e32 v238, v239
	v_add_f32_e32 v238, v238, v239
	v_lshl_add_u32 v240, s29, 6, v218
	v_lshlrev_b32_e32 v241, 3, v201
	v_or_b32_e32 v241, 0x24400, v241
	v_lshl_add_u32 v241, s29, 6, v241
	s_and_saveexec_b64 s[2:3], s[4:5]
	ds_write_b32 v240, v238
	s_or_b64 exec, exec, s[2:3]
	s_waitcnt lgkmcnt(0)
	s_barrier
	ds_read2_b32 v[130:131], v241 offset1:4
	ds_read2_b32 v[132:133], v241 offset0:8 offset1:12
	s_waitcnt lgkmcnt(1)
	v_add_f32_e32 v238, v130, v131
	s_waitcnt lgkmcnt(0)
	v_add_f32_e32 v238, v238, v132
	v_add_f32_e32 v238, v238, v133
	v_mul_f32_e32 v238, 0x3b000000, v238
	v_max_f32_e32 v238, 0xda24260, v238
	v_sqrt_f32_e32 v238, v238
	s_nop 0
	v_cmp_ngt_f32_e64 s[2:3], 1.0, v238
	v_cmp_gt_f32_e32 vcc, 1.0, v238
	v_log_f32_e32 v239, v238
	v_mul_f32_e32 v241, 0x44000000, v178
	s_and_saveexec_b64 s[26:27], vcc
	v_add_f32_e32 v221, v221, v241
	v_mov_b32_e32 v171, v252
	v_mov_b32_e32 v173, v166
	v_mov_b32_e32 v170, v253
	v_mov_b32_e32 v172, v167
	v_mov_b32_e32 v169, v254
	v_mov_b32_e32 v175, v176
	v_mov_b32_e32 v168, v255
	v_mov_b32_e32 v174, v177
	s_or_b64 exec, exec, s[26:27]
	v_mov_b32_e32 v240, 0x41200000
	s_nop 0
	v_cndmask_b32_e64 v240, v240, 1.0, s[22:23]
	s_xor_b32 s29, s29, 1
	s_add_i32 s30, s30, 1
	v_mul_f32_e32 v239, 0xbe4ccccd, v239
	v_exp_f32_e32 v239, v239
	s_nop 0
	v_mul_f32_e32 v239, 0x3f666666, v239
	v_min_f32_e32 v240, v239, v240
	v_max_f32_e32 v239, 0x3e4ccccd, v239
	v_cndmask_b32_e64 v239, v240, v239, s[2:3]
	v_mul_f32_e32 v1, v241, v239
	s_mov_b64 s[22:23], s[2:3]
	s_branch .Lrk_top
